# speedup vs baseline: 1.0856x; 1.0041x over previous
.Lagg_loop:
	s_waitcnt vmcnt(4)
	s_mov_b32 s24, s0
	s_min_i32 s24, s24, s20
	s_mul_i32 s24, s24, s44
	s_add_i32 s24, s24, s45
	s_lshl_b32 s24, s24, 4
	v_add_u32_e32 v33, s24, v18
	v_cmp_gt_i32_e64 s[28:29], s17, v33
	s_add_i32 s24, s0, 16
	s_min_i32 s24, s24, s20
	s_mul_i32 s24, s24, s44
	s_add_i32 s24, s24, s45
	s_lshl_b32 s24, s24, 4
	s_ashr_i32 s25, s24, 31
	v_cndmask_b32_e64 v31, v59, v30, s[28:29]
	v_lshl_add_u64 v[32:33], s[24:25], 2, v[20:21]
	global_load_dword v30, v[32:33], off
	s_waitcnt vmcnt(4)
	v_ashrrev_i32_e32 v32, 17, v29
	v_mul_i32_i24_e32 v32, 0x140, v32
	v_fma_mix_f32 v33, v2, v22, s23 op_sel_hi:[1,0,0]
	v_fma_mix_f32 v34, v2, v22, s23 op_sel:[1,0,0] op_sel_hi:[1,0,0]
	v_or_b32_e32 v32, v23, v32
	v_lshl_add_u32 v33, v34, 16, v33
	ds_add_u32 v32, v33
	v_fma_mix_f32 v33, v3, v22, s23 op_sel_hi:[1,0,0]
	v_fma_mix_f32 v34, v3, v22, s23 op_sel:[1,0,0] op_sel_hi:[1,0,0]
	s_nop 0
	v_lshl_add_u32 v33, v34, 16, v33
	ds_add_u32 v32, v33 offset:64
	v_fma_mix_f32 v33, v4, v22, s23 op_sel_hi:[1,0,0]
	v_fma_mix_f32 v34, v4, v22, s23 op_sel:[1,0,0] op_sel_hi:[1,0,0]
	s_nop 0
	v_lshl_add_u32 v33, v34, 16, v33
	ds_add_u32 v32, v33 offset:128
	v_fma_mix_f32 v33, v5, v22, s23 op_sel_hi:[1,0,0]
	v_fma_mix_f32 v34, v5, v22, s23 op_sel:[1,0,0] op_sel_hi:[1,0,0]
	s_nop 0
	v_lshl_add_u32 v33, v34, 16, v33
	ds_add_u32 v32, v33 offset:192
	v_mov_b32_e32 v29, 0
	s_nop 1
	v_mov_b32_dpp v29, v31 row_newbcast:0 row_mask:0xf bank_mask:0xf
	v_lshlrev_b32_e32 v35, 8, v29
	v_and_or_b32 v35, v35, s22, v24
	s_waitcnt vmcnt(2)
	global_load_dwordx4 v[2:5], v35, s[12:13]
	s_waitcnt vmcnt(4)
	v_ashrrev_i32_e32 v32, 17, v27
	v_mul_i32_i24_e32 v32, 0x140, v32
	v_fma_mix_f32 v33, v6, v22, s23 op_sel_hi:[1,0,0]
	v_fma_mix_f32 v34, v6, v22, s23 op_sel:[1,0,0] op_sel_hi:[1,0,0]
	v_or_b32_e32 v32, v23, v32
	v_lshl_add_u32 v33, v34, 16, v33
	ds_add_u32 v32, v33
	v_fma_mix_f32 v33, v7, v22, s23 op_sel_hi:[1,0,0]
	v_fma_mix_f32 v34, v7, v22, s23 op_sel:[1,0,0] op_sel_hi:[1,0,0]
	s_nop 0
	v_lshl_add_u32 v33, v34, 16, v33
	ds_add_u32 v32, v33 offset:64
	v_fma_mix_f32 v33, v8, v22, s23 op_sel_hi:[1,0,0]
	v_fma_mix_f32 v34, v8, v22, s23 op_sel:[1,0,0] op_sel_hi:[1,0,0]
	s_nop 0
	v_lshl_add_u32 v33, v34, 16, v33
	ds_add_u32 v32, v33 offset:128
	v_fma_mix_f32 v33, v9, v22, s23 op_sel_hi:[1,0,0]
	v_fma_mix_f32 v34, v9, v22, s23 op_sel:[1,0,0] op_sel_hi:[1,0,0]
	s_nop 0
	v_lshl_add_u32 v33, v34, 16, v33
	ds_add_u32 v32, v33 offset:192
	v_mov_b32_e32 v27, 0
	s_nop 1
	v_mov_b32_dpp v27, v31 row_newbcast:1 row_mask:0xf bank_mask:0xf
	v_lshlrev_b32_e32 v35, 8, v27
	v_and_or_b32 v35, v35, s22, v24
	s_waitcnt vmcnt(1)
	global_load_dwordx4 v[6:9], v35, s[12:13]
	s_waitcnt vmcnt(4)
	v_ashrrev_i32_e32 v32, 17, v28
	v_mul_i32_i24_e32 v32, 0x140, v32
	v_fma_mix_f32 v33, v10, v22, s23 op_sel_hi:[1,0,0]
	v_fma_mix_f32 v34, v10, v22, s23 op_sel:[1,0,0] op_sel_hi:[1,0,0]
	v_or_b32_e32 v32, v23, v32
	v_lshl_add_u32 v33, v34, 16, v33
	ds_add_u32 v32, v33
	v_fma_mix_f32 v33, v11, v22, s23 op_sel_hi:[1,0,0]
	v_fma_mix_f32 v34, v11, v22, s23 op_sel:[1,0,0] op_sel_hi:[1,0,0]
	s_nop 0
	v_lshl_add_u32 v33, v34, 16, v33
	ds_add_u32 v32, v33 offset:64
	v_fma_mix_f32 v33, v12, v22, s23 op_sel_hi:[1,0,0]
	v_fma_mix_f32 v34, v12, v22, s23 op_sel:[1,0,0] op_sel_hi:[1,0,0]
	s_nop 0
	v_lshl_add_u32 v33, v34, 16, v33
	ds_add_u32 v32, v33 offset:128
	v_fma_mix_f32 v33, v13, v22, s23 op_sel_hi:[1,0,0]
	v_fma_mix_f32 v34, v13, v22, s23 op_sel:[1,0,0] op_sel_hi:[1,0,0]
	s_nop 0
	v_lshl_add_u32 v33, v34, 16, v33
	ds_add_u32 v32, v33 offset:192
	v_mov_b32_e32 v28, 0
	s_nop 1
	v_mov_b32_dpp v28, v31 row_newbcast:2 row_mask:0xf bank_mask:0xf
	v_lshlrev_b32_e32 v35, 8, v28
	v_and_or_b32 v35, v35, s22, v24
	s_waitcnt vmcnt(1)
	global_load_dwordx4 v[10:13], v35, s[12:13]
	s_waitcnt vmcnt(4)
	v_ashrrev_i32_e32 v32, 17, v26
	v_mul_i32_i24_e32 v32, 0x140, v32
	v_fma_mix_f32 v33, v14, v22, s23 op_sel_hi:[1,0,0]
	v_fma_mix_f32 v34, v14, v22, s23 op_sel:[1,0,0] op_sel_hi:[1,0,0]
	v_or_b32_e32 v32, v23, v32
	v_lshl_add_u32 v33, v34, 16, v33
	ds_add_u32 v32, v33
	v_fma_mix_f32 v33, v15, v22, s23 op_sel_hi:[1,0,0]
	v_fma_mix_f32 v34, v15, v22, s23 op_sel:[1,0,0] op_sel_hi:[1,0,0]
	s_nop 0
	v_lshl_add_u32 v33, v34, 16, v33
	ds_add_u32 v32, v33 offset:64
	v_fma_mix_f32 v33, v16, v22, s23 op_sel_hi:[1,0,0]
	v_fma_mix_f32 v34, v16, v22, s23 op_sel:[1,0,0] op_sel_hi:[1,0,0]
	s_nop 0
	v_lshl_add_u32 v33, v34, 16, v33
	ds_add_u32 v32, v33 offset:128
	v_fma_mix_f32 v33, v17, v22, s23 op_sel_hi:[1,0,0]
	v_fma_mix_f32 v34, v17, v22, s23 op_sel:[1,0,0] op_sel_hi:[1,0,0]
	s_nop 0
	v_lshl_add_u32 v33, v34, 16, v33
	ds_add_u32 v32, v33 offset:192
	v_mov_b32_e32 v26, 0
	s_nop 1
	v_mov_b32_dpp v26, v31 row_newbcast:3 row_mask:0xf bank_mask:0xf
	v_lshlrev_b32_e32 v35, 8, v26
	v_and_or_b32 v35, v35, s22, v24
	s_waitcnt vmcnt(1)
	global_load_dwordx4 v[14:17], v35, s[12:13]
	s_add_i32 s1, s1, 1
	s_add_i32 s0, s0, 16
	s_cmp_lt_u32 s1, s21
	s_cbranch_scc1 .Lagg_loop
